# grid barrier: XCD leader adds to TOP without return and every workgroup polls TOP directly (drops TOP round trip, TOPGEN and XGEN hops); on top of LN1 preload + router LDS prefetch
# speedup vs baseline: 1.0004x; 1.0004x over previous
; #define LAS __attribute__((address_space(3)))
; template <class T> __device__ __forceinline__ T* opaque_p(T* p) { asm volatile("" : "+s"(p)); return p; }
; __device__ __forceinline__ int tidx(int wid) { int l; asm volatile("v_mbcnt_lo_u32_b32 %0, -1, 0\n\tv_mbcnt_hi_u32_b32 %0, -1, %0" : "=v"(l)); return (wid << 6) + l; }
; __device__ __forceinline__ int opaque_s(int v) { asm volatile("" : "+s"(v)); return v; }
; __device__ __forceinline__ unsigned xb_add(unsigned* p, unsigned v) { return __hip_atomic_fetch_add(p, v, __ATOMIC_RELAXED, __HIP_MEMORY_SCOPE_AGENT); }
; #define SEAM(k) do { if (IN(k) && IN((k) + 1)) for (int _r = 0; _r < SEAM_REP; ++_r) xcd_barrier(bar, wid0); } while (0)
; __device__ __forceinline__ void xcd_barrier(const XcdBarrier& b, int wid0) {
;     ...
;             (void)xb_add(&bar[XB_XGEN(b.x)], 1u);
;             __builtin_amdgcn_fence(__ATOMIC_ACQUIRE, "agent");
;             asm volatile("s_waitcnt vmcnt(0)" ::: "memory");
; __global__ void __launch_bounds__(NTHREADS, 2) hybrid_fwd(Args a) {
;     ...
;     XcdBarrier bar = xcd_barrier_post(ctl + CW_BAR, MISC + 8);
;     SEAM(0);
;     ...
;     if (blockIdx.x == 0 && tid == 0) __hip_atomic_store(ctl + CW_FLAG, 0u, __ATOMIC_RELAXED, __HIP_MEMORY_SCOPE_AGENT);
;     ...
;     for (int l = 0; l < NLAYER; ++l) {
;         const int pb = 1 + l * NPH;
;         if (PHEN(1) && IN(pb + 0)) for (int rep = 0; rep < NREP(1); ++rep) { unsigned char* ws = opaque_p(a.ws); LAS unsigned char* lds = opaque_p(lds0); const int bid = opaque_s((int)blockIdx.x); const int tid = tidx(wid0), lane = tid & 63, wave = __builtin_amdgcn_readfirstlane(tid >> 6), gw = bid * NWAVES + wave; (void)lane; (void)gw;
;             pg8::Gemm g{ws, (unsigned)WS_XB, (unsigned)(WS_WIN + (size_t)l * DIN * DM), DM / 2, DM / 2, opaque_s(DM / 2)};
;             pg8::GridOrder S; S.init(MTOK, DIN, DM / 2, DM / 2, G, bid);
;             EpiZ E{(bf16_t*)(ws + WS_Z), (const float*)(ws + WS_COS), (const float*)(ws + WS_SIN)};
;             pg8::gemm_phase<EpiZ, pg8::GridOrder, true, true>(lds, g, S, E, wid0);
;             if (l + 1 < NLAYER && G == 256 && bid >= 128)
.LBB0_165:
	s_or_b64 exec, exec, s[2:3]
	s_load_dwordx4 s[4:7], s[0:1], 0xe0
	s_ashr_i32 s82, s81, 31
	s_cmpk_eq_i32 s81, 0x100
	s_cselect_b64 s[96:97], -1, 0
	s_lshl_b32 s0, s33, 6
	s_waitcnt lgkmcnt(0)
	v_writelane_b32 v255, s4, 6
	s_sub_i32 s86, 0, s0
	s_lshl_b32 s36, s81, 4
	v_writelane_b32 v255, s5, 7
	v_writelane_b32 v255, s6, 8
	v_writelane_b32 v255, s7, 9
	s_movk_i32 s83, 0x2000
	v_readlane_b32 s0, v255, 5
	s_lshl_b32 s91, s0, 6
	s_add_i32 s0, s81, 0xffffff80
	v_writelane_b32 v255, s0, 10
	s_ashr_i32 s0, s0, 31
	v_writelane_b32 v255, s0, 11
	s_lshl_b32 s0, s81, 1
	v_writelane_b32 v255, s0, 12
	s_and_b32 s0, s81, 7
	s_cmp_lg_u32 s0, 0
	s_cselect_b64 s[0:1], -1, 0
	v_writelane_b32 v255, s0, 13
	s_ashr_i32 s37, s36, 31
	s_lshl_b32 s94, s81, 5
	v_writelane_b32 v255, s1, 14
	s_ashr_i32 s0, s81, 3
	v_writelane_b32 v255, s0, 15
	s_lshl_b32 s0, s81, 6
	v_writelane_b32 v255, s0, 16
	s_add_i32 s0, 0, 0x20620
	v_writelane_b32 v255, s0, 17
	s_add_i32 s0, 0, 0x20624
	v_writelane_b32 v255, s0, 18
	s_lshl_b64 s[0:1], s[36:37], 11
	v_writelane_b32 v255, s0, 19
	s_mov_b32 s59, 0x20000
	s_brev_b32 s58, -2
	v_writelane_b32 v255, s1, 20
	s_lshl_b64 s[0:1], s[36:37], 13
	v_writelane_b32 v255, s0, 21
	s_mov_b32 s87, 0xa000
	s_mov_b32 s70, 0xc000
	v_writelane_b32 v255, s1, 22
	s_lshl_b64 s[0:1], s[36:37], 12
	v_writelane_b32 v255, s0, 23
	v_mov_b32_e32 v193, 0
	s_movk_i32 s85, 0x2800
	v_writelane_b32 v255, s1, 24
	v_writelane_b32 v255, s78, 25
	v_writelane_b32 v255, s79, 26
	v_writelane_b32 v255, s82, 27
	v_writelane_b32 v255, s96, 28
	v_mov_b32_e32 v206, 1
	s_movk_i32 s62, 0x5000
	v_writelane_b32 v255, s97, 29
	v_writelane_b32 v255, s86, 30
	v_writelane_b32 v255, s91, 31
	v_writelane_b32 v255, s94, 32
	v_writelane_b32 v255, s60, 33
	s_mov_b32 s69, 0xc3e00000
	s_movk_i32 s33, 0x1000
	v_writelane_b32 v255, s61, 34
	v_writelane_b32 v255, s36, 35
	s_mov_b32 s89, 0xff800000
	s_brev_b32 s68, -3
	s_mov_b32 s52, 0x41000000
	s_movk_i32 s63, 0x7000
	s_mov_b32 s76, 0xf000
	v_mov_b32_e32 v207, 0x3727c5ac
	v_mov_b32_e32 v208, 0x43e00000
	v_mov_b32_e32 v209, 8
	v_mov_b32_e32 v210, 0xff800000
	v_mov_b32_e32 v211, 0xd800
	v_mov_b32_e32 v241, 0x7f800000
	v_mov_b32_e32 v254, 0x50000
	v_mov_b32_e32 v214, 0x2800
	v_mov_b64_e32 v[212:213], 0x100
	s_mov_b32 s80, 0x3d000000
	s_mov_b32 s84, 0x3e0293ee
	s_mov_b32 s88, 0x3b800000
	s_mov_b32 s90, 0x3fd744fd
	s_mov_b32 s72, 0x3d800000
	s_mov_b32 s66, s93
	v_writelane_b32 v255, s37, 36
	s_branch .LBB0_169
.LBB0_167:
	s_or_b64 exec, exec, s[30:31]
	s_barrier

; template <class T> __device__ __forceinline__ T* opaque_p(T* p) { asm volatile("" : "+s"(p)); return p; }
; __device__ __forceinline__ int tidx(int wid) { int l; asm volatile("v_mbcnt_lo_u32_b32 %0, -1, 0\n\tv_mbcnt_hi_u32_b32 %0, -1, %0" : "=v"(l)); return (wid << 6) + l; }
; __device__ __forceinline__ unsigned xb_ld(unsigned* p)              { return __hip_atomic_load(p, __ATOMIC_RELAXED, __HIP_MEMORY_SCOPE_AGENT); }
; __device__ __forceinline__ unsigned xb_add(unsigned* p, unsigned v) { return __hip_atomic_fetch_add(p, v, __ATOMIC_RELAXED, __HIP_MEMORY_SCOPE_AGENT); }
; #define XB_SPIN(cond, bar) do { unsigned _sp = 0; while (cond) { __builtin_amdgcn_s_sleep(1); \
;     if ((++_sp & 255u) == 0u) { if (xb_ld(&(bar)[XB_TMO])) break; if (_sp > XB_SPIN_CAP) { atomicAdd(&(bar)[XB_TMO], 1u); break; } } } } while (0)
; __device__ __forceinline__ void xcd_barrier(const XcdBarrier& b, int wid0) {
;     asm volatile("s_waitcnt vmcnt(0)" ::: "memory");
;     __syncthreads();
;     if (tidx(wid0) == 0) {
;         unsigned* bar = opaque_p(b.bar);
;         __builtin_amdgcn_s_waitcnt(0);
;         unsigned nloc = b.st[0], nx = b.st[1];
;         if (nloc == 0u) { xcd_barrier_complete(bar, b.x, nloc, nx); b.st[0] = nloc; b.st[1] = nx; }
;         const unsigned old = xb_add(&bar[XB_XSUB(b.x)], 1u);
;         const unsigned gen = old / nloc;
;         if (old + 1u == (gen + 1u) * nloc) {
;             __builtin_amdgcn_fence(__ATOMIC_RELEASE, "agent");
;             asm volatile("s_waitcnt vmcnt(0)" ::: "memory");
;             const unsigned og = xb_add(&bar[XB_TOP], 1u);
;             const unsigned tg = og / nx;
;             if (og + 1u == (tg + 1u) * nx) xb_add(&bar[XB_TOPGEN], 1u);
;             else XB_SPIN(xb_ld(&bar[XB_TOPGEN]) == tg, bar);
;             (void)xb_add(&bar[XB_XGEN(b.x)], 1u);
;             __builtin_amdgcn_fence(__ATOMIC_ACQUIRE, "agent");
;             asm volatile("s_waitcnt vmcnt(0)" ::: "memory");
;         } else {
;             XB_SPIN(xb_ld(&bar[XB_XGEN(b.x)]) == gen, bar);
;             __builtin_amdgcn_fence(__ATOMIC_ACQUIRE, "agent");
;             asm volatile("s_waitcnt vmcnt(0)" ::: "memory");
;         }
;     }
;     __syncthreads();
; }
.LBB0_284:
	s_or_b32 s36, s77, 2
	s_cmp_ge_i32 s36, s61
	s_cbranch_scc1 .LBB0_330
	s_waitcnt vmcnt(0)
	s_waitcnt vmcnt(0) lgkmcnt(0)
	s_barrier
	v_mbcnt_lo_u32_b32 v0, -1, 0
	v_mbcnt_hi_u32_b32 v0, -1, v0
	s_nop 0
	v_cmp_eq_u32_e32 vcc, s86, v0
	s_and_saveexec_b64 s[30:31], vcc
	s_cbranch_execz .LBB0_329
	v_readlane_b32 s34, v255, 3
	v_readlane_b32 s0, v255, 17
	v_readlane_b32 s35, v255, 4
	v_readlane_b32 s1, v255, 18
	s_lshl_b32 s2, s91, 2
	s_add_u32 s2, s34, s2
	s_addc_u32 s3, s35, 0
	s_add_u32 s4, s2, 0x1400
	s_addc_u32 s5, s3, 0
	s_add_u32 s6, s34, 0x3400
	s_addc_u32 s7, s35, 0
	v_mov_b32_e32 v0, s0
	v_mov_b32_e32 v1, s1
	ds_read_b32 v2, v0
	ds_read_b32 v12, v1
	v_mov_b32_e32 v6, 1
	v_mov_b32_e32 v8, s4
	v_mov_b32_e32 v9, s5
	v_mov_b32_e32 v10, s6
	v_mov_b32_e32 v11, s7
	s_nop 0
	global_atomic_add v3, v[8:9], v6, off sc0
	s_waitcnt lgkmcnt(0)
	v_cvt_f32_u32_e32 v1, v2
	v_sub_u32_e32 v4, 0, v2
	v_rcp_iflag_f32_e32 v1, v1
	s_nop 0
	v_mul_f32_e32 v1, 0x4f7ffffe, v1
	v_cvt_u32_f32_e32 v1, v1
	v_mul_lo_u32 v4, v4, v1
	v_mul_hi_u32 v4, v1, v4
	v_add_u32_e32 v1, v1, v4
	s_mov_b32 s8, 0
	s_waitcnt vmcnt(0)
	v_mul_hi_u32 v1, v3, v1
	v_mul_lo_u32 v4, v1, v2
	v_sub_u32_e32 v4, v3, v4
	v_cmp_ge_u32_e32 vcc, v4, v2
	v_add_u32_e32 v5, 1, v1
	s_nop 1
	v_cndmask_b32_e32 v1, v1, v5, vcc
	v_sub_u32_e32 v5, v4, v2
	v_cndmask_b32_e32 v4, v4, v5, vcc
	v_cmp_ge_u32_e32 vcc, v4, v2
	v_add_u32_e32 v4, 1, v1
	s_nop 1
	v_cndmask_b32_e32 v1, v1, v4, vcc
	v_add_u32_e32 v1, 1, v1
	v_add_u32_e32 v4, 1, v3
	v_mul_lo_u32 v7, v1, v2
	v_mul_lo_u32 v13, v1, v12
	v_cmp_ne_u32_e32 vcc, v4, v7
	s_nop 1
	s_cbranch_vccnz .Lxb0_poll
	buffer_wbl2 sc1
	s_waitcnt vmcnt(0)
	global_atomic_add v[10:11], v6, off
.Lxb0_poll:
	global_load_dword v14, v[10:11], off sc1
	s_add_i32 s8, s8, 1
	s_waitcnt vmcnt(0)
	v_cmp_lt_u32_e32 vcc, v14, v13
	s_nop 1
	s_cbranch_vccz .Lxb0_done
	s_cmp_lt_u32 s8, 0x40000
	s_cbranch_scc0 .Lxb0_done
	s_sleep 1
	s_branch .Lxb0_poll
.Lxb0_done:
	buffer_inv sc1
	s_waitcnt vmcnt(0)
.LBB0_329:
	s_or_b64 exec, exec, s[30:31]
	s_barrier

; template <class T> __device__ __forceinline__ T* opaque_p(T* p) { asm volatile("" : "+s"(p)); return p; }
; __device__ __forceinline__ int tidx(int wid) { int l; asm volatile("v_mbcnt_lo_u32_b32 %0, -1, 0\n\tv_mbcnt_hi_u32_b32 %0, -1, %0" : "=v"(l)); return (wid << 6) + l; }
; __device__ __forceinline__ unsigned xb_ld(unsigned* p)              { return __hip_atomic_load(p, __ATOMIC_RELAXED, __HIP_MEMORY_SCOPE_AGENT); }
; __device__ __forceinline__ unsigned xb_add(unsigned* p, unsigned v) { return __hip_atomic_fetch_add(p, v, __ATOMIC_RELAXED, __HIP_MEMORY_SCOPE_AGENT); }
; #define XB_SPIN(cond, bar) do { unsigned _sp = 0; while (cond) { __builtin_amdgcn_s_sleep(1); \
;     if ((++_sp & 255u) == 0u) { if (xb_ld(&(bar)[XB_TMO])) break; if (_sp > XB_SPIN_CAP) { atomicAdd(&(bar)[XB_TMO], 1u); break; } } } } while (0)
; __device__ __forceinline__ void xcd_barrier(const XcdBarrier& b, int wid0) {
;     asm volatile("s_waitcnt vmcnt(0)" ::: "memory");
;     __syncthreads();
;     if (tidx(wid0) == 0) {
;         unsigned* bar = opaque_p(b.bar);
;         __builtin_amdgcn_s_waitcnt(0);
;         unsigned nloc = b.st[0], nx = b.st[1];
;         if (nloc == 0u) { xcd_barrier_complete(bar, b.x, nloc, nx); b.st[0] = nloc; b.st[1] = nx; }
;         const unsigned old = xb_add(&bar[XB_XSUB(b.x)], 1u);
;         const unsigned gen = old / nloc;
;         if (old + 1u == (gen + 1u) * nloc) {
;             __builtin_amdgcn_fence(__ATOMIC_RELEASE, "agent");
;             asm volatile("s_waitcnt vmcnt(0)" ::: "memory");
;             const unsigned og = xb_add(&bar[XB_TOP], 1u);
;             const unsigned tg = og / nx;
;             if (og + 1u == (tg + 1u) * nx) xb_add(&bar[XB_TOPGEN], 1u);
;             else XB_SPIN(xb_ld(&bar[XB_TOPGEN]) == tg, bar);
;             (void)xb_add(&bar[XB_XGEN(b.x)], 1u);
;             __builtin_amdgcn_fence(__ATOMIC_ACQUIRE, "agent");
;             asm volatile("s_waitcnt vmcnt(0)" ::: "memory");
;         } else {
;             XB_SPIN(xb_ld(&bar[XB_XGEN(b.x)]) == gen, bar);
;             __builtin_amdgcn_fence(__ATOMIC_ACQUIRE, "agent");
;             asm volatile("s_waitcnt vmcnt(0)" ::: "memory");
;         }
;     }
;     __syncthreads();
; }
.LBB0_521:
	s_or_b32 s36, s77, 3
	s_cmp_lt_i32 s36, s61
	s_cbranch_scc0 .LBB0_567
	s_waitcnt vmcnt(0)
	s_barrier
	v_mbcnt_lo_u32_b32 v0, -1, 0
	v_mbcnt_hi_u32_b32 v0, -1, v0
	s_nop 0
	v_cmp_eq_u32_e32 vcc, s86, v0
	s_and_saveexec_b64 s[30:31], vcc
	s_cbranch_execz .LBB0_566
	v_readlane_b32 s34, v255, 3
	v_readlane_b32 s0, v255, 17
	v_readlane_b32 s35, v255, 4
	v_readlane_b32 s1, v255, 18
	s_lshl_b32 s2, s91, 2
	s_add_u32 s2, s34, s2
	s_addc_u32 s3, s35, 0
	s_add_u32 s4, s2, 0x1400
	s_addc_u32 s5, s3, 0
	s_add_u32 s6, s34, 0x3400
	s_addc_u32 s7, s35, 0
	v_mov_b32_e32 v0, s0
	v_mov_b32_e32 v1, s1
	ds_read_b32 v2, v0
	ds_read_b32 v12, v1
	v_mov_b32_e32 v6, 1
	v_mov_b32_e32 v8, s4
	v_mov_b32_e32 v9, s5
	v_mov_b32_e32 v10, s6
	v_mov_b32_e32 v11, s7
	s_nop 0
	global_atomic_add v3, v[8:9], v6, off sc0
	s_waitcnt lgkmcnt(0)
	v_cvt_f32_u32_e32 v1, v2
	v_sub_u32_e32 v4, 0, v2
	v_rcp_iflag_f32_e32 v1, v1
	s_nop 0
	v_mul_f32_e32 v1, 0x4f7ffffe, v1
	v_cvt_u32_f32_e32 v1, v1
	v_mul_lo_u32 v4, v4, v1
	v_mul_hi_u32 v4, v1, v4
	v_add_u32_e32 v1, v1, v4
	s_mov_b32 s8, 0
	s_waitcnt vmcnt(0)
	v_mul_hi_u32 v1, v3, v1
	v_mul_lo_u32 v4, v1, v2
	v_sub_u32_e32 v4, v3, v4
	v_cmp_ge_u32_e32 vcc, v4, v2
	v_add_u32_e32 v5, 1, v1
	s_nop 1
	v_cndmask_b32_e32 v1, v1, v5, vcc
	v_sub_u32_e32 v5, v4, v2
	v_cndmask_b32_e32 v4, v4, v5, vcc
	v_cmp_ge_u32_e32 vcc, v4, v2
	v_add_u32_e32 v4, 1, v1
	s_nop 1
	v_cndmask_b32_e32 v1, v1, v4, vcc
	v_add_u32_e32 v1, 1, v1
	v_add_u32_e32 v4, 1, v3
	v_mul_lo_u32 v7, v1, v2
	v_mul_lo_u32 v13, v1, v12
	v_cmp_ne_u32_e32 vcc, v4, v7
	s_nop 1
	s_cbranch_vccnz .Lxb1_poll
	buffer_wbl2 sc1
	s_waitcnt vmcnt(0)
	global_atomic_add v[10:11], v6, off

; __device__ __forceinline__ unsigned xb_ld(unsigned* p)              { return __hip_atomic_load(p, __ATOMIC_RELAXED, __HIP_MEMORY_SCOPE_AGENT); }
; __device__ __forceinline__ unsigned xb_add(unsigned* p, unsigned v) { return __hip_atomic_fetch_add(p, v, __ATOMIC_RELAXED, __HIP_MEMORY_SCOPE_AGENT); }
; #define XB_SPIN(cond, bar) do { unsigned _sp = 0; while (cond) { __builtin_amdgcn_s_sleep(1); \
;     if ((++_sp & 255u) == 0u) { if (xb_ld(&(bar)[XB_TMO])) break; if (_sp > XB_SPIN_CAP) { atomicAdd(&(bar)[XB_TMO], 1u); break; } } } } while (0)
; __device__ __forceinline__ void xcd_barrier(const XcdBarrier& b, int wid0) {
;     ...
;             else XB_SPIN(xb_ld(&bar[XB_TOPGEN]) == tg, bar);
;             (void)xb_add(&bar[XB_XGEN(b.x)], 1u);
;             __builtin_amdgcn_fence(__ATOMIC_ACQUIRE, "agent");
;             asm volatile("s_waitcnt vmcnt(0)" ::: "memory");
;         } else {
;             XB_SPIN(xb_ld(&bar[XB_XGEN(b.x)]) == gen, bar);
;             __builtin_amdgcn_fence(__ATOMIC_ACQUIRE, "agent");
;             asm volatile("s_waitcnt vmcnt(0)" ::: "memory");
;         }
.Lxb1_done:
	buffer_inv sc1
	s_waitcnt vmcnt(0)
.LBB0_566:
	s_or_b64 exec, exec, s[30:31]
	s_barrier

; template <class T> __device__ __forceinline__ T* opaque_p(T* p) { asm volatile("" : "+s"(p)); return p; }
; __device__ __forceinline__ int tidx(int wid) { int l; asm volatile("v_mbcnt_lo_u32_b32 %0, -1, 0\n\tv_mbcnt_hi_u32_b32 %0, -1, %0" : "=v"(l)); return (wid << 6) + l; }
; __device__ __forceinline__ unsigned xb_ld(unsigned* p)              { return __hip_atomic_load(p, __ATOMIC_RELAXED, __HIP_MEMORY_SCOPE_AGENT); }
; __device__ __forceinline__ unsigned xb_add(unsigned* p, unsigned v) { return __hip_atomic_fetch_add(p, v, __ATOMIC_RELAXED, __HIP_MEMORY_SCOPE_AGENT); }
; #define XB_SPIN(cond, bar) do { unsigned _sp = 0; while (cond) { __builtin_amdgcn_s_sleep(1); \
;     if ((++_sp & 255u) == 0u) { if (xb_ld(&(bar)[XB_TMO])) break; if (_sp > XB_SPIN_CAP) { atomicAdd(&(bar)[XB_TMO], 1u); break; } } } } while (0)
; __device__ __forceinline__ void xcd_barrier(const XcdBarrier& b, int wid0) {
;     asm volatile("s_waitcnt vmcnt(0)" ::: "memory");
;     __syncthreads();
;     if (tidx(wid0) == 0) {
;         unsigned* bar = opaque_p(b.bar);
;         __builtin_amdgcn_s_waitcnt(0);
;         unsigned nloc = b.st[0], nx = b.st[1];
;         if (nloc == 0u) { xcd_barrier_complete(bar, b.x, nloc, nx); b.st[0] = nloc; b.st[1] = nx; }
;         const unsigned old = xb_add(&bar[XB_XSUB(b.x)], 1u);
;         const unsigned gen = old / nloc;
;         if (old + 1u == (gen + 1u) * nloc) {
;             __builtin_amdgcn_fence(__ATOMIC_RELEASE, "agent");
;             asm volatile("s_waitcnt vmcnt(0)" ::: "memory");
;             const unsigned og = xb_add(&bar[XB_TOP], 1u);
;             const unsigned tg = og / nx;
;             if (og + 1u == (tg + 1u) * nx) xb_add(&bar[XB_TOPGEN], 1u);
;             else XB_SPIN(xb_ld(&bar[XB_TOPGEN]) == tg, bar);
;             (void)xb_add(&bar[XB_XGEN(b.x)], 1u);
;             __builtin_amdgcn_fence(__ATOMIC_ACQUIRE, "agent");
;             asm volatile("s_waitcnt vmcnt(0)" ::: "memory");
;         } else {
;             XB_SPIN(xb_ld(&bar[XB_XGEN(b.x)]) == gen, bar);
;             __builtin_amdgcn_fence(__ATOMIC_ACQUIRE, "agent");
;             asm volatile("s_waitcnt vmcnt(0)" ::: "memory");
;         }
;     }
;     __syncthreads();
; }
.LBB0_698:
	s_add_i32 s0, s77, 4
	s_cmp_ge_i32 s0, s61
	s_cbranch_scc1 .LBB0_744
	s_waitcnt vmcnt(0)
	s_waitcnt vmcnt(0) lgkmcnt(0)
	s_barrier
	v_mbcnt_lo_u32_b32 v0, -1, 0
	v_mbcnt_hi_u32_b32 v0, -1, v0
	s_nop 0
	v_cmp_eq_u32_e32 vcc, s86, v0
	s_and_saveexec_b64 s[30:31], vcc
	s_cbranch_execz .LBB0_743
	v_readlane_b32 s34, v255, 3
	v_readlane_b32 s0, v255, 17
	v_readlane_b32 s35, v255, 4
	v_readlane_b32 s1, v255, 18
	s_lshl_b32 s2, s91, 2
	s_add_u32 s2, s34, s2
	s_addc_u32 s3, s35, 0
	s_add_u32 s4, s2, 0x1400
	s_addc_u32 s5, s3, 0
	s_add_u32 s6, s34, 0x3400
	s_addc_u32 s7, s35, 0
	v_mov_b32_e32 v0, s0
	v_mov_b32_e32 v1, s1
	ds_read_b32 v2, v0
	ds_read_b32 v12, v1
	v_mov_b32_e32 v6, 1
	v_mov_b32_e32 v8, s4
	v_mov_b32_e32 v9, s5
	v_mov_b32_e32 v10, s6
	v_mov_b32_e32 v11, s7
	s_nop 0
	global_atomic_add v3, v[8:9], v6, off sc0
	s_waitcnt lgkmcnt(0)
	v_cvt_f32_u32_e32 v1, v2
	v_sub_u32_e32 v4, 0, v2
	v_rcp_iflag_f32_e32 v1, v1
	s_nop 0
	v_mul_f32_e32 v1, 0x4f7ffffe, v1
	v_cvt_u32_f32_e32 v1, v1
	v_mul_lo_u32 v4, v4, v1
	v_mul_hi_u32 v4, v1, v4
	v_add_u32_e32 v1, v1, v4
	s_mov_b32 s8, 0
	s_waitcnt vmcnt(0)
	v_mul_hi_u32 v1, v3, v1
	v_mul_lo_u32 v4, v1, v2
	v_sub_u32_e32 v4, v3, v4
	v_cmp_ge_u32_e32 vcc, v4, v2
	v_add_u32_e32 v5, 1, v1
	s_nop 1
	v_cndmask_b32_e32 v1, v1, v5, vcc
	v_sub_u32_e32 v5, v4, v2
	v_cndmask_b32_e32 v4, v4, v5, vcc
	v_cmp_ge_u32_e32 vcc, v4, v2
	v_add_u32_e32 v4, 1, v1
	s_nop 1
	v_cndmask_b32_e32 v1, v1, v4, vcc
	v_add_u32_e32 v1, 1, v1
	v_add_u32_e32 v4, 1, v3
	v_mul_lo_u32 v7, v1, v2
	v_mul_lo_u32 v13, v1, v12
	v_cmp_ne_u32_e32 vcc, v4, v7
	s_nop 1
	s_cbranch_vccnz .Lxb2_poll
	buffer_wbl2 sc1
	s_waitcnt vmcnt(0)
	global_atomic_add v[10:11], v6, off

; __device__ __forceinline__ unsigned xb_ld(unsigned* p)              { return __hip_atomic_load(p, __ATOMIC_RELAXED, __HIP_MEMORY_SCOPE_AGENT); }
; __device__ __forceinline__ unsigned xb_add(unsigned* p, unsigned v) { return __hip_atomic_fetch_add(p, v, __ATOMIC_RELAXED, __HIP_MEMORY_SCOPE_AGENT); }
; #define XB_SPIN(cond, bar) do { unsigned _sp = 0; while (cond) { __builtin_amdgcn_s_sleep(1); \
;     if ((++_sp & 255u) == 0u) { if (xb_ld(&(bar)[XB_TMO])) break; if (_sp > XB_SPIN_CAP) { atomicAdd(&(bar)[XB_TMO], 1u); break; } } } } while (0)
; __device__ __forceinline__ void xcd_barrier(const XcdBarrier& b, int wid0) {
;     ...
;             else XB_SPIN(xb_ld(&bar[XB_TOPGEN]) == tg, bar);
;             (void)xb_add(&bar[XB_XGEN(b.x)], 1u);
;             __builtin_amdgcn_fence(__ATOMIC_ACQUIRE, "agent");
;             asm volatile("s_waitcnt vmcnt(0)" ::: "memory");
;         } else {
;             XB_SPIN(xb_ld(&bar[XB_XGEN(b.x)]) == gen, bar);
;             __builtin_amdgcn_fence(__ATOMIC_ACQUIRE, "agent");
;             asm volatile("s_waitcnt vmcnt(0)" ::: "memory");
;         }
.Lxb2_done:
	buffer_inv sc1
	s_waitcnt vmcnt(0)
.LBB0_743:
	s_or_b64 exec, exec, s[30:31]
	s_barrier

; template <class T> __device__ __forceinline__ T* opaque_p(T* p) { asm volatile("" : "+s"(p)); return p; }
; __device__ __forceinline__ int tidx(int wid) { int l; asm volatile("v_mbcnt_lo_u32_b32 %0, -1, 0\n\tv_mbcnt_hi_u32_b32 %0, -1, %0" : "=v"(l)); return (wid << 6) + l; }
; __device__ __forceinline__ unsigned xb_ld(unsigned* p)              { return __hip_atomic_load(p, __ATOMIC_RELAXED, __HIP_MEMORY_SCOPE_AGENT); }
; __device__ __forceinline__ unsigned xb_add(unsigned* p, unsigned v) { return __hip_atomic_fetch_add(p, v, __ATOMIC_RELAXED, __HIP_MEMORY_SCOPE_AGENT); }
; #define XB_SPIN(cond, bar) do { unsigned _sp = 0; while (cond) { __builtin_amdgcn_s_sleep(1); \
;     if ((++_sp & 255u) == 0u) { if (xb_ld(&(bar)[XB_TMO])) break; if (_sp > XB_SPIN_CAP) { atomicAdd(&(bar)[XB_TMO], 1u); break; } } } } while (0)
; __device__ __forceinline__ void xcd_barrier(const XcdBarrier& b, int wid0) {
;     asm volatile("s_waitcnt vmcnt(0)" ::: "memory");
;     __syncthreads();
;     if (tidx(wid0) == 0) {
;         unsigned* bar = opaque_p(b.bar);
;         __builtin_amdgcn_s_waitcnt(0);
;         unsigned nloc = b.st[0], nx = b.st[1];
;         if (nloc == 0u) { xcd_barrier_complete(bar, b.x, nloc, nx); b.st[0] = nloc; b.st[1] = nx; }
;         const unsigned old = xb_add(&bar[XB_XSUB(b.x)], 1u);
;         const unsigned gen = old / nloc;
;         if (old + 1u == (gen + 1u) * nloc) {
;             __builtin_amdgcn_fence(__ATOMIC_RELEASE, "agent");
;             asm volatile("s_waitcnt vmcnt(0)" ::: "memory");
;             const unsigned og = xb_add(&bar[XB_TOP], 1u);
;             const unsigned tg = og / nx;
;             if (og + 1u == (tg + 1u) * nx) xb_add(&bar[XB_TOPGEN], 1u);
;             else XB_SPIN(xb_ld(&bar[XB_TOPGEN]) == tg, bar);
;             (void)xb_add(&bar[XB_XGEN(b.x)], 1u);
;             __builtin_amdgcn_fence(__ATOMIC_ACQUIRE, "agent");
;             asm volatile("s_waitcnt vmcnt(0)" ::: "memory");
;         } else {
;             XB_SPIN(xb_ld(&bar[XB_XGEN(b.x)]) == gen, bar);
;             __builtin_amdgcn_fence(__ATOMIC_ACQUIRE, "agent");
;             asm volatile("s_waitcnt vmcnt(0)" ::: "memory");
;         }
;     }
;     __syncthreads();
; }
.LBB0_759:
	v_readlane_b32 s0, v255, 33
	s_add_i32 s36, s77, 6
	v_readlane_b32 s1, v255, 34
	s_cmp_lt_i32 s36, s1
	s_cbranch_scc0 .LBB0_772
	s_waitcnt vmcnt(0)
	s_waitcnt lgkmcnt(0)
	s_barrier
	v_mbcnt_lo_u32_b32 v0, -1, 0
	v_mbcnt_hi_u32_b32 v0, -1, v0
	s_nop 0
	v_cmp_eq_u32_e32 vcc, s86, v0
	s_and_saveexec_b64 s[30:31], vcc
	s_mov_b32 s93, s61
	v_readlane_b32 s96, v255, 28
	v_readlane_b32 s60, v255, 33
	v_readlane_b32 s97, v255, 29
	v_readlane_b32 s94, v255, 32
	v_readlane_b32 s61, v255, 34
	s_cbranch_execz .LBB0_805
	v_readlane_b32 s34, v255, 3
	v_readlane_b32 s0, v255, 17
	v_readlane_b32 s35, v255, 4
	v_readlane_b32 s1, v255, 18
	s_lshl_b32 s2, s91, 2
	s_add_u32 s2, s34, s2
	s_addc_u32 s3, s35, 0
	s_add_u32 s4, s2, 0x1400
	s_addc_u32 s5, s3, 0
	s_add_u32 s6, s34, 0x3400
	s_addc_u32 s7, s35, 0
	v_mov_b32_e32 v0, s0
	v_mov_b32_e32 v1, s1
	ds_read_b32 v2, v0
	ds_read_b32 v12, v1
	v_mov_b32_e32 v6, 1
	v_mov_b32_e32 v8, s4
	v_mov_b32_e32 v9, s5
	v_mov_b32_e32 v10, s6
	v_mov_b32_e32 v11, s7
	s_nop 0
	global_atomic_add v3, v[8:9], v6, off sc0
	s_waitcnt lgkmcnt(0)
	v_cvt_f32_u32_e32 v1, v2
	v_sub_u32_e32 v4, 0, v2
	v_rcp_iflag_f32_e32 v1, v1
	s_nop 0
	v_mul_f32_e32 v1, 0x4f7ffffe, v1
	v_cvt_u32_f32_e32 v1, v1
	v_mul_lo_u32 v4, v4, v1
	v_mul_hi_u32 v4, v1, v4
	v_add_u32_e32 v1, v1, v4
	s_mov_b32 s8, 0
	s_waitcnt vmcnt(0)
	v_mul_hi_u32 v1, v3, v1
	v_mul_lo_u32 v4, v1, v2
	v_sub_u32_e32 v4, v3, v4
	v_cmp_ge_u32_e32 vcc, v4, v2
	v_add_u32_e32 v5, 1, v1
	s_nop 1
	v_cndmask_b32_e32 v1, v1, v5, vcc
	v_sub_u32_e32 v5, v4, v2
	v_cndmask_b32_e32 v4, v4, v5, vcc
	v_cmp_ge_u32_e32 vcc, v4, v2
	v_add_u32_e32 v4, 1, v1
	s_nop 1
	v_cndmask_b32_e32 v1, v1, v4, vcc
	v_add_u32_e32 v1, 1, v1
	v_add_u32_e32 v4, 1, v3
	v_mul_lo_u32 v7, v1, v2
	v_mul_lo_u32 v13, v1, v12
	v_cmp_ne_u32_e32 vcc, v4, v7
	s_nop 1
	s_cbranch_vccnz .Lxb3_poll
	buffer_wbl2 sc1
	s_waitcnt vmcnt(0)
	global_atomic_add v[10:11], v6, off

; __device__ __forceinline__ unsigned xb_ld(unsigned* p)              { return __hip_atomic_load(p, __ATOMIC_RELAXED, __HIP_MEMORY_SCOPE_AGENT); }
; __device__ __forceinline__ unsigned xb_add(unsigned* p, unsigned v) { return __hip_atomic_fetch_add(p, v, __ATOMIC_RELAXED, __HIP_MEMORY_SCOPE_AGENT); }
; #define XB_SPIN(cond, bar) do { unsigned _sp = 0; while (cond) { __builtin_amdgcn_s_sleep(1); \
;     if ((++_sp & 255u) == 0u) { if (xb_ld(&(bar)[XB_TMO])) break; if (_sp > XB_SPIN_CAP) { atomicAdd(&(bar)[XB_TMO], 1u); break; } } } } while (0)
; __device__ __forceinline__ void xcd_barrier(const XcdBarrier& b, int wid0) {
;     ...
;             else XB_SPIN(xb_ld(&bar[XB_TOPGEN]) == tg, bar);
;             (void)xb_add(&bar[XB_XGEN(b.x)], 1u);
;             __builtin_amdgcn_fence(__ATOMIC_ACQUIRE, "agent");
;             asm volatile("s_waitcnt vmcnt(0)" ::: "memory");
;         } else {
;             XB_SPIN(xb_ld(&bar[XB_XGEN(b.x)]) == gen, bar);
;             __builtin_amdgcn_fence(__ATOMIC_ACQUIRE, "agent");
;             asm volatile("s_waitcnt vmcnt(0)" ::: "memory");
;         }
.Lxb3_done:
	buffer_inv sc1
	s_waitcnt vmcnt(0)
	s_branch .LBB0_805
.LBB0_772:
	s_mov_b32 s93, s61
	v_readlane_b32 s96, v255, 28
	v_readlane_b32 s60, v255, 33
	v_readlane_b32 s97, v255, 29
	v_readlane_b32 s94, v255, 32
	v_readlane_b32 s61, v255, 34
	s_branch .LBB0_806
.LBB0_805:
	s_or_b64 exec, exec, s[30:31]
	s_barrier

; template <class T> __device__ __forceinline__ T* opaque_p(T* p) { asm volatile("" : "+s"(p)); return p; }
; __device__ __forceinline__ int tidx(int wid) { int l; asm volatile("v_mbcnt_lo_u32_b32 %0, -1, 0\n\tv_mbcnt_hi_u32_b32 %0, -1, %0" : "=v"(l)); return (wid << 6) + l; }
; __device__ __forceinline__ unsigned xb_ld(unsigned* p)              { return __hip_atomic_load(p, __ATOMIC_RELAXED, __HIP_MEMORY_SCOPE_AGENT); }
; __device__ __forceinline__ unsigned xb_add(unsigned* p, unsigned v) { return __hip_atomic_fetch_add(p, v, __ATOMIC_RELAXED, __HIP_MEMORY_SCOPE_AGENT); }
; #define XB_SPIN(cond, bar) do { unsigned _sp = 0; while (cond) { __builtin_amdgcn_s_sleep(1); \
;     if ((++_sp & 255u) == 0u) { if (xb_ld(&(bar)[XB_TMO])) break; if (_sp > XB_SPIN_CAP) { atomicAdd(&(bar)[XB_TMO], 1u); break; } } } } while (0)
; __device__ __forceinline__ void xcd_barrier(const XcdBarrier& b, int wid0) {
;     asm volatile("s_waitcnt vmcnt(0)" ::: "memory");
;     __syncthreads();
;     if (tidx(wid0) == 0) {
;         unsigned* bar = opaque_p(b.bar);
;         __builtin_amdgcn_s_waitcnt(0);
;         unsigned nloc = b.st[0], nx = b.st[1];
;         if (nloc == 0u) { xcd_barrier_complete(bar, b.x, nloc, nx); b.st[0] = nloc; b.st[1] = nx; }
;         const unsigned old = xb_add(&bar[XB_XSUB(b.x)], 1u);
;         const unsigned gen = old / nloc;
;         if (old + 1u == (gen + 1u) * nloc) {
;             __builtin_amdgcn_fence(__ATOMIC_RELEASE, "agent");
;             asm volatile("s_waitcnt vmcnt(0)" ::: "memory");
;             const unsigned og = xb_add(&bar[XB_TOP], 1u);
;             const unsigned tg = og / nx;
;             if (og + 1u == (tg + 1u) * nx) xb_add(&bar[XB_TOPGEN], 1u);
;             else XB_SPIN(xb_ld(&bar[XB_TOPGEN]) == tg, bar);
;             (void)xb_add(&bar[XB_XGEN(b.x)], 1u);
;             __builtin_amdgcn_fence(__ATOMIC_ACQUIRE, "agent");
;             asm volatile("s_waitcnt vmcnt(0)" ::: "memory");
;         } else {
;             XB_SPIN(xb_ld(&bar[XB_XGEN(b.x)]) == gen, bar);
;             __builtin_amdgcn_fence(__ATOMIC_ACQUIRE, "agent");
;             asm volatile("s_waitcnt vmcnt(0)" ::: "memory");
;         }
;     }
;     __syncthreads();
; }
.LBB0_835:
	s_add_i32 s36, s77, 7
	s_cmp_ge_i32 s36, s61
	s_cbranch_scc1 .LBB0_881
	s_waitcnt vmcnt(0)
	s_waitcnt lgkmcnt(0)
	s_barrier
	v_mbcnt_lo_u32_b32 v0, -1, 0
	v_mbcnt_hi_u32_b32 v0, -1, v0
	s_nop 0
	v_cmp_eq_u32_e32 vcc, s86, v0
	s_and_saveexec_b64 s[30:31], vcc
	s_cbranch_execz .LBB0_880
	v_readlane_b32 s34, v255, 3
	v_readlane_b32 s0, v255, 17
	v_readlane_b32 s35, v255, 4
	v_readlane_b32 s1, v255, 18
	s_lshl_b32 s2, s91, 2
	s_add_u32 s2, s34, s2
	s_addc_u32 s3, s35, 0
	s_add_u32 s4, s2, 0x1400
	s_addc_u32 s5, s3, 0
	s_add_u32 s6, s34, 0x3400
	s_addc_u32 s7, s35, 0
	v_mov_b32_e32 v0, s0
	v_mov_b32_e32 v1, s1
	ds_read_b32 v2, v0
	ds_read_b32 v12, v1
	v_mov_b32_e32 v6, 1
	v_mov_b32_e32 v8, s4
	v_mov_b32_e32 v9, s5
	v_mov_b32_e32 v10, s6
	v_mov_b32_e32 v11, s7
	s_nop 0
	global_atomic_add v3, v[8:9], v6, off sc0
	s_waitcnt lgkmcnt(0)
	v_cvt_f32_u32_e32 v1, v2
	v_sub_u32_e32 v4, 0, v2
	v_rcp_iflag_f32_e32 v1, v1
	s_nop 0
	v_mul_f32_e32 v1, 0x4f7ffffe, v1
	v_cvt_u32_f32_e32 v1, v1
	v_mul_lo_u32 v4, v4, v1
	v_mul_hi_u32 v4, v1, v4
	v_add_u32_e32 v1, v1, v4
	s_mov_b32 s8, 0
	s_waitcnt vmcnt(0)
	v_mul_hi_u32 v1, v3, v1
	v_mul_lo_u32 v4, v1, v2
	v_sub_u32_e32 v4, v3, v4
	v_cmp_ge_u32_e32 vcc, v4, v2
	v_add_u32_e32 v5, 1, v1
	s_nop 1
	v_cndmask_b32_e32 v1, v1, v5, vcc
	v_sub_u32_e32 v5, v4, v2
	v_cndmask_b32_e32 v4, v4, v5, vcc
	v_cmp_ge_u32_e32 vcc, v4, v2
	v_add_u32_e32 v4, 1, v1
	s_nop 1
	v_cndmask_b32_e32 v1, v1, v4, vcc
	v_add_u32_e32 v1, 1, v1
	v_add_u32_e32 v4, 1, v3
	v_mul_lo_u32 v7, v1, v2
	v_mul_lo_u32 v13, v1, v12
	v_cmp_ne_u32_e32 vcc, v4, v7
	s_nop 1
	s_cbranch_vccnz .Lxb4_poll
	buffer_wbl2 sc1
	s_waitcnt vmcnt(0)
	global_atomic_add v[10:11], v6, off

; __device__ __forceinline__ unsigned xb_ld(unsigned* p)              { return __hip_atomic_load(p, __ATOMIC_RELAXED, __HIP_MEMORY_SCOPE_AGENT); }
; __device__ __forceinline__ unsigned xb_add(unsigned* p, unsigned v) { return __hip_atomic_fetch_add(p, v, __ATOMIC_RELAXED, __HIP_MEMORY_SCOPE_AGENT); }
; #define XB_SPIN(cond, bar) do { unsigned _sp = 0; while (cond) { __builtin_amdgcn_s_sleep(1); \
;     if ((++_sp & 255u) == 0u) { if (xb_ld(&(bar)[XB_TMO])) break; if (_sp > XB_SPIN_CAP) { atomicAdd(&(bar)[XB_TMO], 1u); break; } } } } while (0)
; __device__ __forceinline__ void xcd_barrier(const XcdBarrier& b, int wid0) {
;     ...
;             else XB_SPIN(xb_ld(&bar[XB_TOPGEN]) == tg, bar);
;             (void)xb_add(&bar[XB_XGEN(b.x)], 1u);
;             __builtin_amdgcn_fence(__ATOMIC_ACQUIRE, "agent");
;             asm volatile("s_waitcnt vmcnt(0)" ::: "memory");
;         } else {
;             XB_SPIN(xb_ld(&bar[XB_XGEN(b.x)]) == gen, bar);
;             __builtin_amdgcn_fence(__ATOMIC_ACQUIRE, "agent");
;             asm volatile("s_waitcnt vmcnt(0)" ::: "memory");
;         }
.Lxb4_done:
	buffer_inv sc1
	s_waitcnt vmcnt(0)
.LBB0_880:
	s_or_b64 exec, exec, s[30:31]
	s_barrier

; template <class T> __device__ __forceinline__ T* opaque_p(T* p) { asm volatile("" : "+s"(p)); return p; }
; __device__ __forceinline__ int tidx(int wid) { int l; asm volatile("v_mbcnt_lo_u32_b32 %0, -1, 0\n\tv_mbcnt_hi_u32_b32 %0, -1, %0" : "=v"(l)); return (wid << 6) + l; }
; __device__ __forceinline__ unsigned xb_ld(unsigned* p)              { return __hip_atomic_load(p, __ATOMIC_RELAXED, __HIP_MEMORY_SCOPE_AGENT); }
; __device__ __forceinline__ unsigned xb_add(unsigned* p, unsigned v) { return __hip_atomic_fetch_add(p, v, __ATOMIC_RELAXED, __HIP_MEMORY_SCOPE_AGENT); }
; #define XB_SPIN(cond, bar) do { unsigned _sp = 0; while (cond) { __builtin_amdgcn_s_sleep(1); \
;     if ((++_sp & 255u) == 0u) { if (xb_ld(&(bar)[XB_TMO])) break; if (_sp > XB_SPIN_CAP) { atomicAdd(&(bar)[XB_TMO], 1u); break; } } } } while (0)
; __device__ __forceinline__ void xcd_barrier(const XcdBarrier& b, int wid0) {
;     asm volatile("s_waitcnt vmcnt(0)" ::: "memory");
;     __syncthreads();
;     if (tidx(wid0) == 0) {
;         unsigned* bar = opaque_p(b.bar);
;         __builtin_amdgcn_s_waitcnt(0);
;         unsigned nloc = b.st[0], nx = b.st[1];
;         if (nloc == 0u) { xcd_barrier_complete(bar, b.x, nloc, nx); b.st[0] = nloc; b.st[1] = nx; }
;         const unsigned old = xb_add(&bar[XB_XSUB(b.x)], 1u);
;         const unsigned gen = old / nloc;
;         if (old + 1u == (gen + 1u) * nloc) {
;             __builtin_amdgcn_fence(__ATOMIC_RELEASE, "agent");
;             asm volatile("s_waitcnt vmcnt(0)" ::: "memory");
;             const unsigned og = xb_add(&bar[XB_TOP], 1u);
;             const unsigned tg = og / nx;
;             if (og + 1u == (tg + 1u) * nx) xb_add(&bar[XB_TOPGEN], 1u);
;             else XB_SPIN(xb_ld(&bar[XB_TOPGEN]) == tg, bar);
;             (void)xb_add(&bar[XB_XGEN(b.x)], 1u);
;             __builtin_amdgcn_fence(__ATOMIC_ACQUIRE, "agent");
;             asm volatile("s_waitcnt vmcnt(0)" ::: "memory");
;         } else {
;             XB_SPIN(xb_ld(&bar[XB_XGEN(b.x)]) == gen, bar);
;             __builtin_amdgcn_fence(__ATOMIC_ACQUIRE, "agent");
;             asm volatile("s_waitcnt vmcnt(0)" ::: "memory");
;         }
;     }
;     __syncthreads();
; }
.LBB0_934:
	s_add_i32 s0, s77, 8
	s_cmp_lt_i32 s0, s61
	s_cselect_b64 s[0:1], -1, 0
	s_and_b64 s[0:1], s[20:21], s[0:1]
	s_andn2_b64 vcc, exec, s[0:1]
	s_cbranch_vccnz .LBB0_980
	s_waitcnt vmcnt(0)
	s_waitcnt vmcnt(0) lgkmcnt(0)
	s_barrier
	v_mbcnt_lo_u32_b32 v0, -1, 0
	v_mbcnt_hi_u32_b32 v0, -1, v0
	s_nop 0
	v_cmp_eq_u32_e32 vcc, s86, v0
	s_and_saveexec_b64 s[30:31], vcc
	s_cbranch_execz .LBB0_979
	v_readlane_b32 s34, v255, 3
	v_readlane_b32 s0, v255, 17
	v_readlane_b32 s35, v255, 4
	v_readlane_b32 s1, v255, 18
	s_lshl_b32 s2, s91, 2
	s_add_u32 s2, s34, s2
	s_addc_u32 s3, s35, 0
	s_add_u32 s4, s2, 0x1400
	s_addc_u32 s5, s3, 0
	s_add_u32 s6, s34, 0x3400
	s_addc_u32 s7, s35, 0
	v_mov_b32_e32 v0, s0
	v_mov_b32_e32 v1, s1
	ds_read_b32 v2, v0
	ds_read_b32 v12, v1
	v_mov_b32_e32 v6, 1
	v_mov_b32_e32 v8, s4
	v_mov_b32_e32 v9, s5
	v_mov_b32_e32 v10, s6
	v_mov_b32_e32 v11, s7
	s_nop 0
	global_atomic_add v3, v[8:9], v6, off sc0
	s_waitcnt lgkmcnt(0)
	v_cvt_f32_u32_e32 v1, v2
	v_sub_u32_e32 v4, 0, v2
	v_rcp_iflag_f32_e32 v1, v1
	s_nop 0
	v_mul_f32_e32 v1, 0x4f7ffffe, v1
	v_cvt_u32_f32_e32 v1, v1
	v_mul_lo_u32 v4, v4, v1
	v_mul_hi_u32 v4, v1, v4
	v_add_u32_e32 v1, v1, v4
	s_mov_b32 s8, 0
	s_waitcnt vmcnt(0)
	v_mul_hi_u32 v1, v3, v1
	v_mul_lo_u32 v4, v1, v2
	v_sub_u32_e32 v4, v3, v4
	v_cmp_ge_u32_e32 vcc, v4, v2
	v_add_u32_e32 v5, 1, v1
	s_nop 1
	v_cndmask_b32_e32 v1, v1, v5, vcc
	v_sub_u32_e32 v5, v4, v2
	v_cndmask_b32_e32 v4, v4, v5, vcc
	v_cmp_ge_u32_e32 vcc, v4, v2
	v_add_u32_e32 v4, 1, v1
	s_nop 1
	v_cndmask_b32_e32 v1, v1, v4, vcc
	v_add_u32_e32 v1, 1, v1
	v_add_u32_e32 v4, 1, v3
	v_mul_lo_u32 v7, v1, v2
	v_mul_lo_u32 v13, v1, v12
	v_cmp_ne_u32_e32 vcc, v4, v7
	s_nop 1
	s_cbranch_vccnz .Lxb5_poll
	buffer_wbl2 sc1
	s_waitcnt vmcnt(0)
	global_atomic_add v[10:11], v6, off

; __device__ __forceinline__ unsigned xb_ld(unsigned* p)              { return __hip_atomic_load(p, __ATOMIC_RELAXED, __HIP_MEMORY_SCOPE_AGENT); }
; __device__ __forceinline__ unsigned xb_add(unsigned* p, unsigned v) { return __hip_atomic_fetch_add(p, v, __ATOMIC_RELAXED, __HIP_MEMORY_SCOPE_AGENT); }
; #define XB_SPIN(cond, bar) do { unsigned _sp = 0; while (cond) { __builtin_amdgcn_s_sleep(1); \
;     if ((++_sp & 255u) == 0u) { if (xb_ld(&(bar)[XB_TMO])) break; if (_sp > XB_SPIN_CAP) { atomicAdd(&(bar)[XB_TMO], 1u); break; } } } } while (0)
; __device__ __forceinline__ void xcd_barrier(const XcdBarrier& b, int wid0) {
;     ...
;             else XB_SPIN(xb_ld(&bar[XB_TOPGEN]) == tg, bar);
;             (void)xb_add(&bar[XB_XGEN(b.x)], 1u);
;             __builtin_amdgcn_fence(__ATOMIC_ACQUIRE, "agent");
;             asm volatile("s_waitcnt vmcnt(0)" ::: "memory");
;         } else {
;             XB_SPIN(xb_ld(&bar[XB_XGEN(b.x)]) == gen, bar);
;             __builtin_amdgcn_fence(__ATOMIC_ACQUIRE, "agent");
;             asm volatile("s_waitcnt vmcnt(0)" ::: "memory");
;         }
.Lxb5_done:
	buffer_inv sc1
	s_waitcnt vmcnt(0)
.LBB0_979:
	s_or_b64 exec, exec, s[30:31]
	s_barrier

; template <class T> __device__ __forceinline__ T* opaque_p(T* p) { asm volatile("" : "+s"(p)); return p; }
; __device__ __forceinline__ int tidx(int wid) { int l; asm volatile("v_mbcnt_lo_u32_b32 %0, -1, 0\n\tv_mbcnt_hi_u32_b32 %0, -1, %0" : "=v"(l)); return (wid << 6) + l; }
; __device__ __forceinline__ unsigned xb_ld(unsigned* p)              { return __hip_atomic_load(p, __ATOMIC_RELAXED, __HIP_MEMORY_SCOPE_AGENT); }
; __device__ __forceinline__ unsigned xb_add(unsigned* p, unsigned v) { return __hip_atomic_fetch_add(p, v, __ATOMIC_RELAXED, __HIP_MEMORY_SCOPE_AGENT); }
; #define XB_SPIN(cond, bar) do { unsigned _sp = 0; while (cond) { __builtin_amdgcn_s_sleep(1); \
;     if ((++_sp & 255u) == 0u) { if (xb_ld(&(bar)[XB_TMO])) break; if (_sp > XB_SPIN_CAP) { atomicAdd(&(bar)[XB_TMO], 1u); break; } } } } while (0)
; __device__ __forceinline__ void xcd_barrier(const XcdBarrier& b, int wid0) {
;     asm volatile("s_waitcnt vmcnt(0)" ::: "memory");
;     __syncthreads();
;     if (tidx(wid0) == 0) {
;         unsigned* bar = opaque_p(b.bar);
;         __builtin_amdgcn_s_waitcnt(0);
;         unsigned nloc = b.st[0], nx = b.st[1];
;         if (nloc == 0u) { xcd_barrier_complete(bar, b.x, nloc, nx); b.st[0] = nloc; b.st[1] = nx; }
;         const unsigned old = xb_add(&bar[XB_XSUB(b.x)], 1u);
;         const unsigned gen = old / nloc;
;         if (old + 1u == (gen + 1u) * nloc) {
;             __builtin_amdgcn_fence(__ATOMIC_RELEASE, "agent");
;             asm volatile("s_waitcnt vmcnt(0)" ::: "memory");
;             const unsigned og = xb_add(&bar[XB_TOP], 1u);
;             const unsigned tg = og / nx;
;             if (og + 1u == (tg + 1u) * nx) xb_add(&bar[XB_TOPGEN], 1u);
;             else XB_SPIN(xb_ld(&bar[XB_TOPGEN]) == tg, bar);
;             (void)xb_add(&bar[XB_XGEN(b.x)], 1u);
;             __builtin_amdgcn_fence(__ATOMIC_ACQUIRE, "agent");
;             asm volatile("s_waitcnt vmcnt(0)" ::: "memory");
;         } else {
;             XB_SPIN(xb_ld(&bar[XB_XGEN(b.x)]) == gen, bar);
;             __builtin_amdgcn_fence(__ATOMIC_ACQUIRE, "agent");
;             asm volatile("s_waitcnt vmcnt(0)" ::: "memory");
;         }
;     }
;     __syncthreads();
; }
.LBB0_1033:
	s_waitcnt vmcnt(0)
	s_waitcnt vmcnt(0) lgkmcnt(0)
	s_barrier
	v_mbcnt_lo_u32_b32 v0, -1, 0
	v_mbcnt_hi_u32_b32 v0, -1, v0
	s_nop 0
	v_cmp_eq_u32_e32 vcc, s86, v0
	s_and_saveexec_b64 s[30:31], vcc
	s_cbranch_execz .LBB0_1077
	v_readlane_b32 s34, v255, 3
	v_readlane_b32 s0, v255, 17
	v_readlane_b32 s35, v255, 4
	v_readlane_b32 s1, v255, 18
	s_lshl_b32 s2, s91, 2
	s_add_u32 s2, s34, s2
	s_addc_u32 s3, s35, 0
	s_add_u32 s4, s2, 0x1400
	s_addc_u32 s5, s3, 0
	s_add_u32 s6, s34, 0x3400
	s_addc_u32 s7, s35, 0
	v_mov_b32_e32 v0, s0
	v_mov_b32_e32 v1, s1
	ds_read_b32 v2, v0
	ds_read_b32 v12, v1
	v_mov_b32_e32 v6, 1
	v_mov_b32_e32 v8, s4
	v_mov_b32_e32 v9, s5
	v_mov_b32_e32 v10, s6
	v_mov_b32_e32 v11, s7
	s_nop 0
	global_atomic_add v3, v[8:9], v6, off sc0
	s_waitcnt lgkmcnt(0)
	v_cvt_f32_u32_e32 v1, v2
	v_sub_u32_e32 v4, 0, v2
	v_rcp_iflag_f32_e32 v1, v1
	s_nop 0
	v_mul_f32_e32 v1, 0x4f7ffffe, v1
	v_cvt_u32_f32_e32 v1, v1
	v_mul_lo_u32 v4, v4, v1
	v_mul_hi_u32 v4, v1, v4
	v_add_u32_e32 v1, v1, v4
	s_mov_b32 s8, 0
	s_waitcnt vmcnt(0)
	v_mul_hi_u32 v1, v3, v1
	v_mul_lo_u32 v4, v1, v2
	v_sub_u32_e32 v4, v3, v4
	v_cmp_ge_u32_e32 vcc, v4, v2
	v_add_u32_e32 v5, 1, v1
	s_nop 1
	v_cndmask_b32_e32 v1, v1, v5, vcc
	v_sub_u32_e32 v5, v4, v2
	v_cndmask_b32_e32 v4, v4, v5, vcc
	v_cmp_ge_u32_e32 vcc, v4, v2
	v_add_u32_e32 v4, 1, v1
	s_nop 1
	v_cndmask_b32_e32 v1, v1, v4, vcc
	v_add_u32_e32 v1, 1, v1
	v_add_u32_e32 v4, 1, v3
	v_mul_lo_u32 v7, v1, v2
	v_mul_lo_u32 v13, v1, v12
	v_cmp_ne_u32_e32 vcc, v4, v7
	s_nop 1
	s_cbranch_vccnz .Lxb6_poll
	buffer_wbl2 sc1
	s_waitcnt vmcnt(0)
	global_atomic_add v[10:11], v6, off

; __device__ __forceinline__ unsigned xb_ld(unsigned* p)              { return __hip_atomic_load(p, __ATOMIC_RELAXED, __HIP_MEMORY_SCOPE_AGENT); }
; __device__ __forceinline__ unsigned xb_add(unsigned* p, unsigned v) { return __hip_atomic_fetch_add(p, v, __ATOMIC_RELAXED, __HIP_MEMORY_SCOPE_AGENT); }
; #define XB_SPIN(cond, bar) do { unsigned _sp = 0; while (cond) { __builtin_amdgcn_s_sleep(1); \
;     if ((++_sp & 255u) == 0u) { if (xb_ld(&(bar)[XB_TMO])) break; if (_sp > XB_SPIN_CAP) { atomicAdd(&(bar)[XB_TMO], 1u); break; } } } } while (0)
; __device__ __forceinline__ void xcd_barrier(const XcdBarrier& b, int wid0) {
;     ...
;             else XB_SPIN(xb_ld(&bar[XB_TOPGEN]) == tg, bar);
;             (void)xb_add(&bar[XB_XGEN(b.x)], 1u);
;             __builtin_amdgcn_fence(__ATOMIC_ACQUIRE, "agent");
;             asm volatile("s_waitcnt vmcnt(0)" ::: "memory");
;         } else {
;             XB_SPIN(xb_ld(&bar[XB_XGEN(b.x)]) == gen, bar);
;             __builtin_amdgcn_fence(__ATOMIC_ACQUIRE, "agent");
;             asm volatile("s_waitcnt vmcnt(0)" ::: "memory");
;         }
.Lxb6_done:
	buffer_inv sc1
	s_waitcnt vmcnt(0)
.LBB0_1077:
	s_or_b64 exec, exec, s[30:31]
	s_barrier

; template <class T> __device__ __forceinline__ T* opaque_p(T* p) { asm volatile("" : "+s"(p)); return p; }
; __device__ __forceinline__ int tidx(int wid) { int l; asm volatile("v_mbcnt_lo_u32_b32 %0, -1, 0\n\tv_mbcnt_hi_u32_b32 %0, -1, %0" : "=v"(l)); return (wid << 6) + l; }
; __device__ __forceinline__ unsigned xb_ld(unsigned* p)              { return __hip_atomic_load(p, __ATOMIC_RELAXED, __HIP_MEMORY_SCOPE_AGENT); }
; __device__ __forceinline__ unsigned xb_add(unsigned* p, unsigned v) { return __hip_atomic_fetch_add(p, v, __ATOMIC_RELAXED, __HIP_MEMORY_SCOPE_AGENT); }
; #define XB_SPIN(cond, bar) do { unsigned _sp = 0; while (cond) { __builtin_amdgcn_s_sleep(1); \
;     if ((++_sp & 255u) == 0u) { if (xb_ld(&(bar)[XB_TMO])) break; if (_sp > XB_SPIN_CAP) { atomicAdd(&(bar)[XB_TMO], 1u); break; } } } } while (0)
; __device__ __forceinline__ void xcd_barrier(const XcdBarrier& b, int wid0) {
;     asm volatile("s_waitcnt vmcnt(0)" ::: "memory");
;     __syncthreads();
;     if (tidx(wid0) == 0) {
;         unsigned* bar = opaque_p(b.bar);
;         __builtin_amdgcn_s_waitcnt(0);
;         unsigned nloc = b.st[0], nx = b.st[1];
;         if (nloc == 0u) { xcd_barrier_complete(bar, b.x, nloc, nx); b.st[0] = nloc; b.st[1] = nx; }
;         const unsigned old = xb_add(&bar[XB_XSUB(b.x)], 1u);
;         const unsigned gen = old / nloc;
;         if (old + 1u == (gen + 1u) * nloc) {
;             __builtin_amdgcn_fence(__ATOMIC_RELEASE, "agent");
;             asm volatile("s_waitcnt vmcnt(0)" ::: "memory");
;             const unsigned og = xb_add(&bar[XB_TOP], 1u);
;             const unsigned tg = og / nx;
;             if (og + 1u == (tg + 1u) * nx) xb_add(&bar[XB_TOPGEN], 1u);
;             else XB_SPIN(xb_ld(&bar[XB_TOPGEN]) == tg, bar);
;             (void)xb_add(&bar[XB_XGEN(b.x)], 1u);
;             __builtin_amdgcn_fence(__ATOMIC_ACQUIRE, "agent");
;             asm volatile("s_waitcnt vmcnt(0)" ::: "memory");
;         } else {
;             XB_SPIN(xb_ld(&bar[XB_XGEN(b.x)]) == gen, bar);
;             __builtin_amdgcn_fence(__ATOMIC_ACQUIRE, "agent");
;             asm volatile("s_waitcnt vmcnt(0)" ::: "memory");
;         }
;     }
;     __syncthreads();
; }
.LBB0_1145:
	s_add_i32 s36, s77, 11
	s_cmp_ge_i32 s36, s61
	s_cbranch_scc1 .LBB0_1191
	s_waitcnt vmcnt(0)
	s_waitcnt vmcnt(0) lgkmcnt(0)
	s_barrier
	v_mbcnt_lo_u32_b32 v0, -1, 0
	v_mbcnt_hi_u32_b32 v0, -1, v0
	s_nop 0
	v_cmp_eq_u32_e32 vcc, s86, v0
	s_and_saveexec_b64 s[30:31], vcc
	s_cbranch_execz .LBB0_1190
	v_readlane_b32 s34, v255, 3
	v_readlane_b32 s0, v255, 17
	v_readlane_b32 s35, v255, 4
	v_readlane_b32 s1, v255, 18
	s_lshl_b32 s2, s91, 2
	s_add_u32 s2, s34, s2
	s_addc_u32 s3, s35, 0
	s_add_u32 s4, s2, 0x1400
	s_addc_u32 s5, s3, 0
	s_add_u32 s6, s34, 0x3400
	s_addc_u32 s7, s35, 0
	v_mov_b32_e32 v0, s0
	v_mov_b32_e32 v1, s1
	ds_read_b32 v2, v0
	ds_read_b32 v12, v1
	v_mov_b32_e32 v6, 1
	v_mov_b32_e32 v8, s4
	v_mov_b32_e32 v9, s5
	v_mov_b32_e32 v10, s6
	v_mov_b32_e32 v11, s7
	s_nop 0
	global_atomic_add v3, v[8:9], v6, off sc0
	s_waitcnt lgkmcnt(0)
	v_cvt_f32_u32_e32 v1, v2
	v_sub_u32_e32 v4, 0, v2
	v_rcp_iflag_f32_e32 v1, v1
	s_nop 0
	v_mul_f32_e32 v1, 0x4f7ffffe, v1
	v_cvt_u32_f32_e32 v1, v1
	v_mul_lo_u32 v4, v4, v1
	v_mul_hi_u32 v4, v1, v4
	v_add_u32_e32 v1, v1, v4
	s_mov_b32 s8, 0
	s_waitcnt vmcnt(0)
	v_mul_hi_u32 v1, v3, v1
	v_mul_lo_u32 v4, v1, v2
	v_sub_u32_e32 v4, v3, v4
	v_cmp_ge_u32_e32 vcc, v4, v2
	v_add_u32_e32 v5, 1, v1
	s_nop 1
	v_cndmask_b32_e32 v1, v1, v5, vcc
	v_sub_u32_e32 v5, v4, v2
	v_cndmask_b32_e32 v4, v4, v5, vcc
	v_cmp_ge_u32_e32 vcc, v4, v2
	v_add_u32_e32 v4, 1, v1
	s_nop 1
	v_cndmask_b32_e32 v1, v1, v4, vcc
	v_add_u32_e32 v1, 1, v1
	v_add_u32_e32 v4, 1, v3
	v_mul_lo_u32 v7, v1, v2
	v_mul_lo_u32 v13, v1, v12
	v_cmp_ne_u32_e32 vcc, v4, v7
	s_nop 1
	s_cbranch_vccnz .Lxb7_poll
	buffer_wbl2 sc1
	s_waitcnt vmcnt(0)
	global_atomic_add v[10:11], v6, off

; __device__ __forceinline__ unsigned xb_ld(unsigned* p)              { return __hip_atomic_load(p, __ATOMIC_RELAXED, __HIP_MEMORY_SCOPE_AGENT); }
; __device__ __forceinline__ unsigned xb_add(unsigned* p, unsigned v) { return __hip_atomic_fetch_add(p, v, __ATOMIC_RELAXED, __HIP_MEMORY_SCOPE_AGENT); }
; #define XB_SPIN(cond, bar) do { unsigned _sp = 0; while (cond) { __builtin_amdgcn_s_sleep(1); \
;     if ((++_sp & 255u) == 0u) { if (xb_ld(&(bar)[XB_TMO])) break; if (_sp > XB_SPIN_CAP) { atomicAdd(&(bar)[XB_TMO], 1u); break; } } } } while (0)
; __device__ __forceinline__ void xcd_barrier(const XcdBarrier& b, int wid0) {
;     ...
;             else XB_SPIN(xb_ld(&bar[XB_TOPGEN]) == tg, bar);
;             (void)xb_add(&bar[XB_XGEN(b.x)], 1u);
;             __builtin_amdgcn_fence(__ATOMIC_ACQUIRE, "agent");
;             asm volatile("s_waitcnt vmcnt(0)" ::: "memory");
;         } else {
;             XB_SPIN(xb_ld(&bar[XB_XGEN(b.x)]) == gen, bar);
;             __builtin_amdgcn_fence(__ATOMIC_ACQUIRE, "agent");
;             asm volatile("s_waitcnt vmcnt(0)" ::: "memory");
;         }
.Lxb7_done:
	buffer_inv sc1
	s_waitcnt vmcnt(0)
.LBB0_1190:
	s_or_b64 exec, exec, s[30:31]
	s_barrier

; template <class T> __device__ __forceinline__ T* opaque_p(T* p) { asm volatile("" : "+s"(p)); return p; }
; __device__ __forceinline__ int tidx(int wid) { int l; asm volatile("v_mbcnt_lo_u32_b32 %0, -1, 0\n\tv_mbcnt_hi_u32_b32 %0, -1, %0" : "=v"(l)); return (wid << 6) + l; }
; __device__ __forceinline__ unsigned xb_ld(unsigned* p)              { return __hip_atomic_load(p, __ATOMIC_RELAXED, __HIP_MEMORY_SCOPE_AGENT); }
; __device__ __forceinline__ unsigned xb_add(unsigned* p, unsigned v) { return __hip_atomic_fetch_add(p, v, __ATOMIC_RELAXED, __HIP_MEMORY_SCOPE_AGENT); }
; #define XB_SPIN(cond, bar) do { unsigned _sp = 0; while (cond) { __builtin_amdgcn_s_sleep(1); \
;     if ((++_sp & 255u) == 0u) { if (xb_ld(&(bar)[XB_TMO])) break; if (_sp > XB_SPIN_CAP) { atomicAdd(&(bar)[XB_TMO], 1u); break; } } } } while (0)
; __device__ __forceinline__ void xcd_barrier(const XcdBarrier& b, int wid0) {
;     asm volatile("s_waitcnt vmcnt(0)" ::: "memory");
;     __syncthreads();
;     if (tidx(wid0) == 0) {
;         unsigned* bar = opaque_p(b.bar);
;         __builtin_amdgcn_s_waitcnt(0);
;         unsigned nloc = b.st[0], nx = b.st[1];
;         if (nloc == 0u) { xcd_barrier_complete(bar, b.x, nloc, nx); b.st[0] = nloc; b.st[1] = nx; }
;         const unsigned old = xb_add(&bar[XB_XSUB(b.x)], 1u);
;         const unsigned gen = old / nloc;
;         if (old + 1u == (gen + 1u) * nloc) {
;             __builtin_amdgcn_fence(__ATOMIC_RELEASE, "agent");
;             asm volatile("s_waitcnt vmcnt(0)" ::: "memory");
;             const unsigned og = xb_add(&bar[XB_TOP], 1u);
;             const unsigned tg = og / nx;
;             if (og + 1u == (tg + 1u) * nx) xb_add(&bar[XB_TOPGEN], 1u);
;             else XB_SPIN(xb_ld(&bar[XB_TOPGEN]) == tg, bar);
;             (void)xb_add(&bar[XB_XGEN(b.x)], 1u);
;             __builtin_amdgcn_fence(__ATOMIC_ACQUIRE, "agent");
;             asm volatile("s_waitcnt vmcnt(0)" ::: "memory");
;         } else {
;             XB_SPIN(xb_ld(&bar[XB_XGEN(b.x)]) == gen, bar);
;             __builtin_amdgcn_fence(__ATOMIC_ACQUIRE, "agent");
;             asm volatile("s_waitcnt vmcnt(0)" ::: "memory");
;         }
;     }
;     __syncthreads();
; }
.LBB0_1284:
	s_add_i32 s36, s77, 12
	s_cmp_ge_i32 s36, s61
	s_cbranch_scc1 .LBB0_1330
	s_waitcnt vmcnt(0)
	s_waitcnt lgkmcnt(0)
	s_barrier
	s_waitcnt vmcnt(0)
	v_mbcnt_lo_u32_b32 v0, -1, 0
	v_mbcnt_hi_u32_b32 v0, -1, v0
	s_nop 0
	v_cmp_eq_u32_e32 vcc, s86, v0
	s_and_saveexec_b64 s[30:31], vcc
	s_cbranch_execz .LBB0_1329
	v_readlane_b32 s34, v255, 3
	v_readlane_b32 s0, v255, 17
	v_readlane_b32 s35, v255, 4
	v_readlane_b32 s1, v255, 18
	s_lshl_b32 s2, s91, 2
	s_add_u32 s2, s34, s2
	s_addc_u32 s3, s35, 0
	s_add_u32 s4, s2, 0x1400
	s_addc_u32 s5, s3, 0
	s_add_u32 s6, s34, 0x3400
	s_addc_u32 s7, s35, 0
	v_mov_b32_e32 v0, s0
	v_mov_b32_e32 v1, s1
	ds_read_b32 v2, v0
	ds_read_b32 v12, v1
	v_mov_b32_e32 v6, 1
	v_mov_b32_e32 v8, s4
	v_mov_b32_e32 v9, s5
	v_mov_b32_e32 v10, s6
	v_mov_b32_e32 v11, s7
	s_nop 0
	global_atomic_add v3, v[8:9], v6, off sc0
	s_waitcnt lgkmcnt(0)
	v_cvt_f32_u32_e32 v1, v2
	v_sub_u32_e32 v4, 0, v2
	v_rcp_iflag_f32_e32 v1, v1
	s_nop 0
	v_mul_f32_e32 v1, 0x4f7ffffe, v1
	v_cvt_u32_f32_e32 v1, v1
	v_mul_lo_u32 v4, v4, v1
	v_mul_hi_u32 v4, v1, v4
	v_add_u32_e32 v1, v1, v4
	s_mov_b32 s8, 0
	s_waitcnt vmcnt(0)
	v_mul_hi_u32 v1, v3, v1
	v_mul_lo_u32 v4, v1, v2
	v_sub_u32_e32 v4, v3, v4
	v_cmp_ge_u32_e32 vcc, v4, v2
	v_add_u32_e32 v5, 1, v1
	s_nop 1
	v_cndmask_b32_e32 v1, v1, v5, vcc
	v_sub_u32_e32 v5, v4, v2
	v_cndmask_b32_e32 v4, v4, v5, vcc
	v_cmp_ge_u32_e32 vcc, v4, v2
	v_add_u32_e32 v4, 1, v1
	s_nop 1
	v_cndmask_b32_e32 v1, v1, v4, vcc
	v_add_u32_e32 v1, 1, v1
	v_add_u32_e32 v4, 1, v3
	v_mul_lo_u32 v7, v1, v2
	v_mul_lo_u32 v13, v1, v12
	v_cmp_ne_u32_e32 vcc, v4, v7
	s_nop 1
	s_cbranch_vccnz .Lxb8_poll
	buffer_wbl2 sc1
	s_waitcnt vmcnt(0)
	global_atomic_add v[10:11], v6, off

; __device__ __forceinline__ unsigned xb_ld(unsigned* p)              { return __hip_atomic_load(p, __ATOMIC_RELAXED, __HIP_MEMORY_SCOPE_AGENT); }
; __device__ __forceinline__ unsigned xb_add(unsigned* p, unsigned v) { return __hip_atomic_fetch_add(p, v, __ATOMIC_RELAXED, __HIP_MEMORY_SCOPE_AGENT); }
; #define XB_SPIN(cond, bar) do { unsigned _sp = 0; while (cond) { __builtin_amdgcn_s_sleep(1); \
;     if ((++_sp & 255u) == 0u) { if (xb_ld(&(bar)[XB_TMO])) break; if (_sp > XB_SPIN_CAP) { atomicAdd(&(bar)[XB_TMO], 1u); break; } } } } while (0)
; __device__ __forceinline__ void xcd_barrier(const XcdBarrier& b, int wid0) {
;     ...
;             else XB_SPIN(xb_ld(&bar[XB_TOPGEN]) == tg, bar);
;             (void)xb_add(&bar[XB_XGEN(b.x)], 1u);
;             __builtin_amdgcn_fence(__ATOMIC_ACQUIRE, "agent");
;             asm volatile("s_waitcnt vmcnt(0)" ::: "memory");
;         } else {
;             XB_SPIN(xb_ld(&bar[XB_XGEN(b.x)]) == gen, bar);
;             __builtin_amdgcn_fence(__ATOMIC_ACQUIRE, "agent");
;             asm volatile("s_waitcnt vmcnt(0)" ::: "memory");
;         }
.Lxb8_done:
	buffer_inv sc1
	s_waitcnt vmcnt(0)
.LBB0_1329:
	s_or_b64 exec, exec, s[30:31]
	s_barrier

; #define SEAM(k) do { if (IN(k) && IN((k) + 1)) for (int _r = 0; _r < SEAM_REP; ++_r) xcd_barrier(bar, wid0); } while (0)
; __global__ void __launch_bounds__(NTHREADS, 2) hybrid_fwd(Args a) {
;     ...
;     for (int l = 0; l < NLAYER; ++l) {
;         const int pb = 1 + l * NPH;
;     ...
;         SEAM(pb + 11);
;     }
.Lxb9_out:
	s_getpc_b64 s[98:99]

; template <class T> __device__ __forceinline__ T* opaque_p(T* p) { asm volatile("" : "+s"(p)); return p; }
; __device__ __forceinline__ int tidx(int wid) { int l; asm volatile("v_mbcnt_lo_u32_b32 %0, -1, 0\n\tv_mbcnt_hi_u32_b32 %0, -1, %0" : "=v"(l)); return (wid << 6) + l; }
; __device__ __forceinline__ unsigned xb_ld(unsigned* p)              { return __hip_atomic_load(p, __ATOMIC_RELAXED, __HIP_MEMORY_SCOPE_AGENT); }
; __device__ __forceinline__ unsigned xb_add(unsigned* p, unsigned v) { return __hip_atomic_fetch_add(p, v, __ATOMIC_RELAXED, __HIP_MEMORY_SCOPE_AGENT); }
; #define XB_SPIN(cond, bar) do { unsigned _sp = 0; while (cond) { __builtin_amdgcn_s_sleep(1); \
;     if ((++_sp & 255u) == 0u) { if (xb_ld(&(bar)[XB_TMO])) break; if (_sp > XB_SPIN_CAP) { atomicAdd(&(bar)[XB_TMO], 1u); break; } } } } while (0)
; __device__ __forceinline__ void xcd_barrier(const XcdBarrier& b, int wid0) {
;     asm volatile("s_waitcnt vmcnt(0)" ::: "memory");
;     __syncthreads();
;     if (tidx(wid0) == 0) {
;         unsigned* bar = opaque_p(b.bar);
;         __builtin_amdgcn_s_waitcnt(0);
;         unsigned nloc = b.st[0], nx = b.st[1];
;         if (nloc == 0u) { xcd_barrier_complete(bar, b.x, nloc, nx); b.st[0] = nloc; b.st[1] = nx; }
;         const unsigned old = xb_add(&bar[XB_XSUB(b.x)], 1u);
;         const unsigned gen = old / nloc;
;         if (old + 1u == (gen + 1u) * nloc) {
;             __builtin_amdgcn_fence(__ATOMIC_RELEASE, "agent");
;             asm volatile("s_waitcnt vmcnt(0)" ::: "memory");
;             const unsigned og = xb_add(&bar[XB_TOP], 1u);
;             const unsigned tg = og / nx;
;             if (og + 1u == (tg + 1u) * nx) xb_add(&bar[XB_TOPGEN], 1u);
;             else XB_SPIN(xb_ld(&bar[XB_TOPGEN]) == tg, bar);
;             (void)xb_add(&bar[XB_XGEN(b.x)], 1u);
;             __builtin_amdgcn_fence(__ATOMIC_ACQUIRE, "agent");
;             asm volatile("s_waitcnt vmcnt(0)" ::: "memory");
;         } else {
;             XB_SPIN(xb_ld(&bar[XB_XGEN(b.x)]) == gen, bar);
;             __builtin_amdgcn_fence(__ATOMIC_ACQUIRE, "agent");
;             asm volatile("s_waitcnt vmcnt(0)" ::: "memory");
;         }
;     }
;     __syncthreads();
; }
.LBB0_1507:
	v_readlane_b32 s34, v255, 3
	v_readlane_b32 s0, v255, 17
	v_readlane_b32 s35, v255, 4
	v_readlane_b32 s1, v255, 18
	s_lshl_b32 s2, s91, 2
	s_add_u32 s2, s34, s2
	s_addc_u32 s3, s35, 0
	s_add_u32 s4, s2, 0x1400
	s_addc_u32 s5, s3, 0
	s_add_u32 s6, s34, 0x3400
	s_addc_u32 s7, s35, 0
	v_mov_b32_e32 v0, s0
	v_mov_b32_e32 v1, s1
	ds_read_b32 v2, v0
	ds_read_b32 v12, v1
	v_mov_b32_e32 v6, 1
	v_mov_b32_e32 v8, s4
	v_mov_b32_e32 v9, s5
	v_mov_b32_e32 v10, s6
	v_mov_b32_e32 v11, s7
	s_nop 0
	global_atomic_add v3, v[8:9], v6, off sc0
	s_waitcnt lgkmcnt(0)
	v_cvt_f32_u32_e32 v1, v2
	v_sub_u32_e32 v4, 0, v2
	v_rcp_iflag_f32_e32 v1, v1
	s_nop 0
	v_mul_f32_e32 v1, 0x4f7ffffe, v1
	v_cvt_u32_f32_e32 v1, v1
	v_mul_lo_u32 v4, v4, v1
	v_mul_hi_u32 v4, v1, v4
	v_add_u32_e32 v1, v1, v4
	s_mov_b32 s8, 0
	s_waitcnt vmcnt(0)
	v_mul_hi_u32 v1, v3, v1
	v_mul_lo_u32 v4, v1, v2
	v_sub_u32_e32 v4, v3, v4
	v_cmp_ge_u32_e32 vcc, v4, v2
	v_add_u32_e32 v5, 1, v1
	s_nop 1
	v_cndmask_b32_e32 v1, v1, v5, vcc
	v_sub_u32_e32 v5, v4, v2
	v_cndmask_b32_e32 v4, v4, v5, vcc
	v_cmp_ge_u32_e32 vcc, v4, v2
	v_add_u32_e32 v4, 1, v1
	s_nop 1
	v_cndmask_b32_e32 v1, v1, v4, vcc
	v_add_u32_e32 v1, 1, v1
	v_add_u32_e32 v4, 1, v3
	v_mul_lo_u32 v7, v1, v2
	v_mul_lo_u32 v13, v1, v12
	v_cmp_ne_u32_e32 vcc, v4, v7
	s_nop 1
	s_cbranch_vccnz .Lxb9_poll
	buffer_wbl2 sc1
	s_waitcnt vmcnt(0)
	global_atomic_add v[10:11], v6, off

; #define SEAM(k) do { if (IN(k) && IN((k) + 1)) for (int _r = 0; _r < SEAM_REP; ++_r) xcd_barrier(bar, wid0); } while (0)
; __global__ void __launch_bounds__(NTHREADS, 2) hybrid_fwd(Args a) {
;     ...
;         SEAM(pb + 11);
;     }
;     ...
; }
.LBB0_1532:
	v_bfe_u32 v132, v145, 4, 1
	v_and_b32_e32 v133, 0x78, v92
	s_cbranch_execz .LBB0_1461
	s_branch .LBB0_1462
.LBB0_1551:
	s_endpgm
